# adds attention row max as two v_max3 chains and lane exchange by permlane swap
# baseline (speedup 1.0000x reference)
.LBB0_334:
	s_nop 10
	v_max3_f32 v2, v82, v83, v84
	v_max3_f32 v4, v98, v99, v100
	v_max3_f32 v2, v2, v85, v86
	v_max3_f32 v4, v4, v101, v102
	v_max3_f32 v2, v2, v87, v88
	v_max3_f32 v4, v4, v103, v104
	v_max3_f32 v2, v2, v89, v90
	v_max3_f32 v4, v4, v105, v106
	v_max3_f32 v2, v2, v91, v92
	v_max3_f32 v4, v4, v107, v108
	v_max3_f32 v2, v2, v93, v94
	v_max3_f32 v4, v4, v109, v110
	v_max3_f32 v2, v2, v95, v96
	v_max3_f32 v4, v4, v111, v112
	v_max3_f32 v2, v2, v97, v113
	v_max_f32_e32 v2, v2, v4
	v_mov_b32_e32 v4, v2
	s_nop 1
	v_permlane32_swap_b32_e32 v2, v4
	v_max_f32_e32 v2, v2, v4
	v_add_f32_e32 v4, 0x41000000, v195
	v_cmp_gt_f32_e32 vcc, v2, v4
	s_cbranch_vccz .LBB0_336
	s_nop 0
	v_cndmask_b32_e32 v4, v195, v2, vcc
	v_sub_f32_e32 v2, v195, v4
	v_exp_f32_e32 v2, v2
	v_mov_b32_e32 v195, v4
	v_pk_mul_f32 v[80:81], v[80:81], v[2:3] op_sel_hi:[1,0]
	v_pk_mul_f32 v[78:79], v[78:79], v[2:3] op_sel_hi:[1,0]
	v_pk_mul_f32 v[76:77], v[76:77], v[2:3] op_sel_hi:[1,0]
	v_pk_mul_f32 v[74:75], v[74:75], v[2:3] op_sel_hi:[1,0]
	v_pk_mul_f32 v[72:73], v[72:73], v[2:3] op_sel_hi:[1,0]
	v_pk_mul_f32 v[70:71], v[70:71], v[2:3] op_sel_hi:[1,0]
	v_pk_mul_f32 v[68:69], v[68:69], v[2:3] op_sel_hi:[1,0]
	v_pk_mul_f32 v[66:67], v[66:67], v[2:3] op_sel_hi:[1,0]
	v_pk_mul_f32 v[64:65], v[64:65], v[2:3] op_sel_hi:[1,0]
	v_pk_mul_f32 v[62:63], v[62:63], v[2:3] op_sel_hi:[1,0]
	v_pk_mul_f32 v[60:61], v[60:61], v[2:3] op_sel_hi:[1,0]
	v_pk_mul_f32 v[58:59], v[58:59], v[2:3] op_sel_hi:[1,0]
	v_pk_mul_f32 v[56:57], v[56:57], v[2:3] op_sel_hi:[1,0]
	v_pk_mul_f32 v[54:55], v[54:55], v[2:3] op_sel_hi:[1,0]
	v_pk_mul_f32 v[52:53], v[52:53], v[2:3] op_sel_hi:[1,0]
	v_pk_mul_f32 v[50:51], v[50:51], v[2:3] op_sel_hi:[1,0]
	v_pk_mul_f32 v[48:49], v[48:49], v[2:3] op_sel_hi:[1,0]
	v_pk_mul_f32 v[46:47], v[46:47], v[2:3] op_sel_hi:[1,0]
	v_pk_mul_f32 v[44:45], v[44:45], v[2:3] op_sel_hi:[1,0]
	v_pk_mul_f32 v[42:43], v[42:43], v[2:3] op_sel_hi:[1,0]
	v_pk_mul_f32 v[40:41], v[40:41], v[2:3] op_sel_hi:[1,0]
	v_pk_mul_f32 v[38:39], v[38:39], v[2:3] op_sel_hi:[1,0]
	v_pk_mul_f32 v[36:37], v[36:37], v[2:3] op_sel_hi:[1,0]
	v_pk_mul_f32 v[34:35], v[34:35], v[2:3] op_sel_hi:[1,0]
	v_pk_mul_f32 v[32:33], v[32:33], v[2:3] op_sel_hi:[1,0]
	v_pk_mul_f32 v[30:31], v[30:31], v[2:3] op_sel_hi:[1,0]
	v_pk_mul_f32 v[28:29], v[28:29], v[2:3] op_sel_hi:[1,0]
	v_pk_mul_f32 v[26:27], v[26:27], v[2:3] op_sel_hi:[1,0]
	v_pk_mul_f32 v[24:25], v[24:25], v[2:3] op_sel_hi:[1,0]
	v_pk_mul_f32 v[22:23], v[22:23], v[2:3] op_sel_hi:[1,0]
	v_pk_mul_f32 v[20:21], v[20:21], v[2:3] op_sel_hi:[1,0]
	v_pk_mul_f32 v[18:19], v[18:19], v[2:3] op_sel_hi:[1,0]
	v_mul_f32_e32 v5, v5, v2
